# speedup vs baseline: 1.0111x; 1.0008x over previous
.LBB5_8:
	s_or_b64 exec, exec, s[38:39]
	v_add_u32_e32 v156, 0x8000, v142
	s_load_dwordx2 s[38:39], s[0:1], 0x78
	s_load_dwordx2 s[44:45], s[0:1], 0x68
	s_load_dwordx2 s[48:49], s[0:1], 0x28
	s_mov_b64 s[0:1], 0x80
	v_readfirstlane_b32 s61, v156
	v_add_u32_e32 v157, 0xa000, v142
	v_lshl_add_u64 v[10:11], v[10:11], 0, s[0:1]
	s_mov_b32 m0, s61
	v_readfirstlane_b32 s61, v157
	s_waitcnt vmcnt(2)
	s_barrier
	global_load_lds_dwordx4 v[10:11], off
	s_mov_b32 m0, s61
	s_add_i32 s61, 0, 0x18000
	v_add_u32_e32 v158, s61, v162
	v_lshl_add_u64 v[8:9], v[8:9], 0, s[0:1]
	v_readfirstlane_b32 s62, v158
	s_add_u32 s56, s56, 0x80080
	global_load_lds_dwordx4 v[8:9], off
	s_mov_b32 m0, s62
	v_add_u32_e32 v159, 0x2000, v158
	s_addc_u32 s57, s57, 0
	s_add_i32 s62, 0, 0x1c000
	v_lshl_add_u64 v[6:7], v[6:7], 0, s[0:1]
	v_lshl_add_u64 v[4:5], v[4:5], 0, s[0:1]
	v_readfirstlane_b32 s0, v159
	v_add_u32_e32 v160, s62, v162
	global_load_lds_dwordx4 v[6:7], off
	s_mov_b32 m0, s0
	v_readfirstlane_b32 s63, v160
	v_add_u32_e32 v161, 0x2000, v160
	global_load_lds_dwordx4 v[4:5], off
	s_mov_b32 m0, s63
	v_readfirstlane_b32 s63, v161
	global_load_lds_dwordx4 v130, s[56:57]
	s_mov_b32 m0, s63
	v_lshlrev_b32_e32 v4, 6, v0
	global_load_lds_dwordx4 v132, s[56:57]
	v_lshlrev_b32_e32 v185, 2, v0
	v_and_b32_e32 v146, 48, v0
	v_and_b32_e32 v5, 0x3c0, v4
	v_and_b32_e32 v152, 32, v185
	v_bitop3_b32 v5, v5, v152, v146 bitop3:0x36
	s_add_u32 s3, s54, s3
	v_add_u32_e32 v8, s35, v5
	s_addc_u32 s35, s55, 0
	s_add_u32 s30, s30, s3
	s_addc_u32 s31, s31, s35
	s_lshl_b32 s2, s2, 16
	v_and_b32_e32 v15, 0x3000, v4
	v_add_u16_e32 v4, v12, v13
	s_and_b32 s2, s2, 0x300000
	v_lshrrev_b16_e32 v6, 1, v4
	v_lshlrev_b32_e32 v4, 8, v0
	v_lshlrev_b32_e32 v7, 4, v164
	s_add_u32 s2, s52, s2
	v_and_b32_e32 v4, 0x18000, v4
	v_lshlrev_b32_e32 v3, 11, v3
	v_and_b32_e32 v7, 0x38000, v7
	s_addc_u32 s3, s53, 0
	s_waitcnt vmcnt(6)
	v_lshlrev_b32_e32 v14, 13, v14
	v_or3_b32 v4, v6, v4, v3
	v_or3_b32 v3, v6, v7, v3
	s_add_u32 s2, s28, s2
	v_add_u32_e32 v9, s60, v5
	v_add_u32_e32 v10, s61, v5
	v_add_u32_e32 v11, s62, v5
	v_add_u32_e32 v16, 0, v5
	v_or_b32_e32 v17, 0x800, v14
	v_or_b32_e32 v18, 0x1000, v14
	v_or_b32_e32 v19, 0x1800, v14
	v_lshlrev_b32_e32 v4, 1, v4
	v_mov_b32_e32 v5, v2
	v_lshlrev_b32_e32 v6, 1, v3
	v_mov_b32_e32 v7, v2
	s_addc_u32 s3, s29, s3
	s_mov_b64 s[0:1], 0x80080
	s_mov_b64 s[96:97], s[2:3]
	s_mov_b64 s[98:99], s[30:31]
	v_mov_b32_e32 v254, v4
	v_mov_b32_e32 v255, v6
	v_lshl_add_u64 v[134:135], s[30:31], 0, v[4:5]
	v_lshl_add_u64 v[136:137], s[30:31], 0, v[6:7]
	v_lshl_add_u64 v[138:139], s[2:3], 0, v[4:5]
	v_lshl_add_u64 v[140:141], s[2:3], 0, v[6:7]
	s_mov_b32 s35, -2
	s_mov_b64 s[2:3], 0
	v_add_u32_e32 v165, v8, v15
	v_add_u32_e32 v150, v16, v14
	v_add_u32_e32 v149, v16, v17
	v_add_u32_e32 v148, v16, v18
	v_add_u32_e32 v147, v16, v19
	v_add_u32_e32 v163, v9, v15
	s_mov_b64 s[28:29], 0x100
	s_mov_b64 s[30:31], 0x80100
	v_add_u32_e32 v133, v10, v15
	s_mov_b64 s[52:53], 0x180
	s_mov_b64 s[54:55], 0x80180
	v_add_u32_e32 v131, v11, v15
	v_mov_b32_e32 v3, v2
	v_mov_b32_e32 v4, v2
	v_mov_b32_e32 v6, v2
	v_mov_b32_e32 v8, v2
	v_mov_b32_e32 v9, v2
	v_mov_b32_e32 v10, v2
	v_mov_b32_e32 v11, v2
	v_mov_b32_e32 v12, v2
	v_mov_b32_e32 v13, v2
	v_mov_b32_e32 v14, v2
	v_mov_b32_e32 v15, v2
	v_mov_b32_e32 v16, v2
	v_mov_b32_e32 v17, v2
	v_mov_b32_e32 v18, v2
	v_mov_b32_e32 v19, v2
	v_mov_b32_e32 v20, v2
	v_mov_b32_e32 v21, v2
	v_mov_b32_e32 v22, v2
	v_mov_b32_e32 v23, v2
	v_mov_b32_e32 v24, v2
	v_mov_b32_e32 v25, v2
	v_mov_b32_e32 v26, v2
	v_mov_b32_e32 v27, v2
	v_mov_b32_e32 v28, v2
	v_mov_b32_e32 v29, v2
	v_mov_b32_e32 v30, v2
	v_mov_b32_e32 v31, v2
	v_mov_b32_e32 v32, v2
	v_mov_b32_e32 v33, v2
	v_mov_b32_e32 v34, v2
	v_mov_b32_e32 v35, v2
	v_mov_b32_e32 v36, v2
	v_mov_b32_e32 v37, v2
	v_mov_b32_e32 v38, v2
	v_mov_b32_e32 v39, v2
	v_mov_b32_e32 v40, v2
	v_mov_b32_e32 v41, v2
	v_mov_b32_e32 v42, v2
	v_mov_b32_e32 v43, v2
	v_mov_b32_e32 v44, v2
	v_mov_b32_e32 v45, v2
	v_mov_b32_e32 v46, v2
	v_mov_b32_e32 v47, v2
	v_mov_b32_e32 v48, v2
	v_mov_b32_e32 v49, v2
	v_mov_b32_e32 v50, v2
	v_mov_b32_e32 v51, v2
	v_mov_b32_e32 v52, v2
	v_mov_b32_e32 v53, v2
	v_mov_b32_e32 v54, v2
	v_mov_b32_e32 v55, v2
	v_mov_b32_e32 v56, v2
	v_mov_b32_e32 v57, v2
	v_mov_b32_e32 v58, v2
	v_mov_b32_e32 v59, v2
	v_mov_b32_e32 v60, v2
	v_mov_b32_e32 v61, v2
	v_mov_b32_e32 v62, v2
	v_mov_b32_e32 v63, v2
	v_mov_b32_e32 v64, v2
	v_mov_b32_e32 v65, v2
	v_mov_b32_e32 v66, v2
	v_mov_b32_e32 v67, v2
	v_mov_b32_e32 v68, v2
	v_mov_b32_e32 v69, v2
	v_mov_b32_e32 v70, v2
	v_mov_b32_e32 v71, v2
	v_mov_b32_e32 v72, v2
	v_mov_b32_e32 v73, v2
	v_mov_b32_e32 v74, v2
	v_mov_b32_e32 v75, v2
	v_mov_b32_e32 v76, v2
	v_mov_b32_e32 v77, v2
	v_mov_b32_e32 v78, v2
	v_mov_b32_e32 v79, v2
	v_mov_b32_e32 v80, v2
	v_mov_b32_e32 v81, v2
	v_mov_b32_e32 v82, v2
	v_mov_b32_e32 v83, v2
	v_mov_b32_e32 v84, v2
	v_mov_b32_e32 v85, v2
	v_mov_b32_e32 v86, v2
	v_mov_b32_e32 v87, v2
	v_mov_b32_e32 v88, v2
	v_mov_b32_e32 v89, v2
	v_mov_b32_e32 v90, v2
	v_mov_b32_e32 v91, v2
	v_mov_b32_e32 v92, v2
	v_mov_b32_e32 v93, v2
	v_mov_b32_e32 v94, v2
	v_mov_b32_e32 v95, v2
	v_mov_b32_e32 v96, v2
	v_mov_b32_e32 v97, v2
	v_mov_b32_e32 v98, v2
	v_mov_b32_e32 v99, v2
	v_mov_b32_e32 v100, v2
	v_mov_b32_e32 v101, v2
	v_mov_b32_e32 v102, v2
	v_mov_b32_e32 v103, v2
	v_mov_b32_e32 v104, v2
	v_mov_b32_e32 v105, v2
	v_mov_b32_e32 v106, v2
	v_mov_b32_e32 v107, v2
	v_mov_b32_e32 v108, v2
	v_mov_b32_e32 v109, v2
	v_mov_b32_e32 v110, v2
	v_mov_b32_e32 v111, v2
	v_mov_b32_e32 v112, v2
	v_mov_b32_e32 v113, v2
	v_mov_b32_e32 v114, v2
	v_mov_b32_e32 v115, v2
	v_mov_b32_e32 v116, v2
	v_mov_b32_e32 v117, v2
	v_mov_b32_e32 v118, v2
	v_mov_b32_e32 v119, v2
	v_mov_b32_e32 v120, v2
	v_mov_b32_e32 v121, v2
	v_mov_b32_e32 v122, v2
	v_mov_b32_e32 v123, v2
	v_mov_b32_e32 v124, v2
	v_mov_b32_e32 v125, v2
	v_mov_b32_e32 v126, v2
	v_mov_b32_e32 v127, v2
	v_mov_b32_e32 v128, v2
	v_mov_b32_e32 v129, v2
	v_lshrrev_b32_e32 v190, 2, v0
	v_and_b32_e32 v186, 48, v162
	v_and_b32_e32 v188, 15, v0
	v_add_u32_e32 v166, 0xc000, v142
	v_add_u32_e32 v167, 0xe000, v142
	s_barrier
	v_readfirstlane_b32 s80, v166
	v_readfirstlane_b32 s81, v167
	v_readfirstlane_b32 s82, v144
	v_readfirstlane_b32 s83, v145
	v_readfirstlane_b32 s84, v142
	v_readfirstlane_b32 s85, v143
	v_readfirstlane_b32 s86, v154
	v_readfirstlane_b32 s87, v155
	v_readfirstlane_b32 s88, v151
	v_readfirstlane_b32 s89, v153
	v_readfirstlane_b32 s90, v158
	v_readfirstlane_b32 s91, v159
	v_readfirstlane_b32 s92, v156
	v_readfirstlane_b32 s93, v157
	v_readfirstlane_b32 s94, v160
	v_readfirstlane_b32 s95, v161
.LBB5_9:
	ds_read_b128 v[168:171], v165
	ds_read_b128 v[172:175], v165 offset:1024
	ds_read_b128 v[176:179], v165 offset:2048
	ds_read_b128 v[192:195], v165 offset:3072
	s_mov_b32 s56, s80
	s_mov_b32 m0, s56
	s_mov_b32 s56, s81
	s_add_u32 s100, s96, s0
	s_addc_u32 s101, s97, s1
	global_load_lds_dwordx4 v254, s[100:101]
	s_mov_b32 m0, s56
	s_nop 0
	global_load_lds_dwordx4 v255, s[100:101]
	ds_read_b128 v[196:199], v150
	ds_read_b128 v[200:203], v150 offset:1024
	ds_read_b128 v[204:207], v149
	ds_read_b128 v[208:211], v149 offset:1024
	ds_read_b128 v[212:215], v148
	ds_read_b128 v[216:219], v148 offset:1024
	ds_read_b128 v[220:223], v147
	ds_read_b128 v[224:227], v147 offset:1024
	s_waitcnt lgkmcnt(8)
	s_barrier
	s_waitcnt lgkmcnt(0)
	s_setprio 1
	s_waitcnt lgkmcnt(0)
	v_mfma_f32_16x16x32_f16 v[126:129], v[168:171], v[196:199], v[126:129]
	v_mfma_f32_16x16x32_f16 v[122:125], v[176:179], v[196:199], v[122:125]
	v_mfma_f32_16x16x32_f16 v[118:121], v[168:171], v[204:207], v[118:121]
	v_mfma_f32_16x16x32_f16 v[114:117], v[176:179], v[204:207], v[114:117]
	v_mfma_f32_16x16x32_f16 v[110:113], v[168:171], v[212:215], v[110:113]
	v_mfma_f32_16x16x32_f16 v[106:109], v[176:179], v[212:215], v[106:109]
	v_mfma_f32_16x16x32_f16 v[102:105], v[168:171], v[220:223], v[102:105]
	v_mfma_f32_16x16x32_f16 v[98:101], v[176:179], v[220:223], v[98:101]
	v_mfma_f32_16x16x32_f16 v[126:129], v[172:175], v[200:203], v[126:129]
	v_mfma_f32_16x16x32_f16 v[122:125], v[192:195], v[200:203], v[122:125]
	v_mfma_f32_16x16x32_f16 v[118:121], v[172:175], v[208:211], v[118:121]
	v_mfma_f32_16x16x32_f16 v[114:117], v[192:195], v[208:211], v[114:117]
	v_mfma_f32_16x16x32_f16 v[110:113], v[172:175], v[216:219], v[110:113]
	v_mfma_f32_16x16x32_f16 v[106:109], v[192:195], v[216:219], v[106:109]
	v_mfma_f32_16x16x32_f16 v[102:105], v[172:175], v[224:227], v[102:105]
	v_mfma_f32_16x16x32_f16 v[98:101], v[192:195], v[224:227], v[98:101]
	s_setprio 0
	s_barrier
	s_mov_b32 s56, s82
	s_mov_b32 m0, s56
	ds_read_b128 v[228:231], v163
	ds_read_b128 v[232:235], v163 offset:1024
	ds_read_b128 v[236:239], v163 offset:2048
	ds_read_b128 v[240:243], v163 offset:3072
	s_add_u32 s100, s98, s28
	s_addc_u32 s101, s99, s29
	global_load_lds_dwordx4 v254, s[100:101]
	s_mov_b32 s56, s83
	s_mov_b32 m0, s56
	s_nop 0
	global_load_lds_dwordx4 v255, s[100:101]
	s_barrier
	s_waitcnt lgkmcnt(0)
	s_setprio 1
	s_waitcnt lgkmcnt(0)
	v_mfma_f32_16x16x32_f16 v[94:97], v[228:231], v[196:199], v[94:97]
	v_mfma_f32_16x16x32_f16 v[90:93], v[236:239], v[196:199], v[90:93]
	v_mfma_f32_16x16x32_f16 v[86:89], v[228:231], v[204:207], v[86:89]
	v_mfma_f32_16x16x32_f16 v[82:85], v[236:239], v[204:207], v[82:85]
	v_mfma_f32_16x16x32_f16 v[78:81], v[228:231], v[212:215], v[78:81]
	v_mfma_f32_16x16x32_f16 v[74:77], v[236:239], v[212:215], v[74:77]
	v_mfma_f32_16x16x32_f16 v[70:73], v[228:231], v[220:223], v[70:73]
	v_mfma_f32_16x16x32_f16 v[66:69], v[236:239], v[220:223], v[66:69]
	v_mfma_f32_16x16x32_f16 v[94:97], v[232:235], v[200:203], v[94:97]
	v_mfma_f32_16x16x32_f16 v[90:93], v[240:243], v[200:203], v[90:93]
	v_mfma_f32_16x16x32_f16 v[86:89], v[232:235], v[208:211], v[86:89]
	v_mfma_f32_16x16x32_f16 v[82:85], v[240:243], v[208:211], v[82:85]
	v_mfma_f32_16x16x32_f16 v[78:81], v[232:235], v[216:219], v[78:81]
	v_mfma_f32_16x16x32_f16 v[74:77], v[240:243], v[216:219], v[74:77]
	v_mfma_f32_16x16x32_f16 v[70:73], v[232:235], v[224:227], v[70:73]
	v_mfma_f32_16x16x32_f16 v[66:69], v[240:243], v[224:227], v[66:69]
	s_setprio 0
	s_mov_b32 s56, s84
	s_mov_b32 m0, s56
	s_mov_b32 s56, s85
	s_barrier
	ds_read_b128 v[196:199], v150 offset:16384
	ds_read_b128 v[200:203], v150 offset:17408
	ds_read_b128 v[204:207], v149 offset:16384
	ds_read_b128 v[208:211], v149 offset:17408
	ds_read_b128 v[212:215], v148 offset:16384
	ds_read_b128 v[216:219], v148 offset:17408
	ds_read_b128 v[220:223], v147 offset:16384
	ds_read_b128 v[224:227], v147 offset:17408
	s_add_u32 s100, s96, s28
	s_addc_u32 s101, s97, s29
	global_load_lds_dwordx4 v254, s[100:101]
	s_mov_b32 m0, s56
	s_nop 0
	global_load_lds_dwordx4 v255, s[100:101]
	s_barrier
	s_waitcnt lgkmcnt(0)
	s_setprio 1
	s_waitcnt lgkmcnt(0)
	v_mfma_f32_16x16x32_f16 v[62:65], v[168:171], v[196:199], v[62:65]
	v_mfma_f32_16x16x32_f16 v[58:61], v[176:179], v[196:199], v[58:61]
	v_mfma_f32_16x16x32_f16 v[54:57], v[168:171], v[204:207], v[54:57]
	v_mfma_f32_16x16x32_f16 v[50:53], v[176:179], v[204:207], v[50:53]
	v_mfma_f32_16x16x32_f16 v[46:49], v[168:171], v[212:215], v[46:49]
	v_mfma_f32_16x16x32_f16 v[42:45], v[176:179], v[212:215], v[42:45]
	v_mfma_f32_16x16x32_f16 v[38:41], v[168:171], v[220:223], v[38:41]
	v_mfma_f32_16x16x32_f16 v[34:37], v[176:179], v[220:223], v[34:37]
	v_mfma_f32_16x16x32_f16 v[62:65], v[172:175], v[200:203], v[62:65]
	v_mfma_f32_16x16x32_f16 v[58:61], v[192:195], v[200:203], v[58:61]
	v_mfma_f32_16x16x32_f16 v[54:57], v[172:175], v[208:211], v[54:57]
	v_mfma_f32_16x16x32_f16 v[50:53], v[192:195], v[208:211], v[50:53]
	v_mfma_f32_16x16x32_f16 v[46:49], v[172:175], v[216:219], v[46:49]
	v_mfma_f32_16x16x32_f16 v[42:45], v[192:195], v[216:219], v[42:45]
	v_mfma_f32_16x16x32_f16 v[38:41], v[172:175], v[224:227], v[38:41]
	v_mfma_f32_16x16x32_f16 v[34:37], v[192:195], v[224:227], v[34:37]
	s_setprio 0
	s_barrier
	s_mov_b32 s56, s86
	s_mov_b32 m0, s56
	s_mov_b32 s56, s87
	s_add_u32 s100, s98, s30
	s_addc_u32 s101, s99, s31
	global_load_lds_dwordx4 v254, s[100:101]
	s_mov_b32 m0, s56
	s_nop 0
	global_load_lds_dwordx4 v255, s[100:101]
	s_waitcnt vmcnt(6)
	s_barrier
	s_setprio 1
	v_mfma_f32_16x16x32_f16 v[30:33], v[228:231], v[196:199], v[30:33]
	v_mfma_f32_16x16x32_f16 v[26:29], v[236:239], v[196:199], v[26:29]
	v_mfma_f32_16x16x32_f16 v[22:25], v[228:231], v[204:207], v[22:25]
	v_mfma_f32_16x16x32_f16 v[18:21], v[236:239], v[204:207], v[18:21]
	v_mfma_f32_16x16x32_f16 v[14:17], v[228:231], v[212:215], v[14:17]
	v_mfma_f32_16x16x32_f16 v[10:13], v[236:239], v[212:215], v[10:13]
	v_mfma_f32_16x16x32_f16 v[6:9], v[228:231], v[220:223], v[6:9]
	v_mfma_f32_16x16x32_f16 v[2:5], v[236:239], v[220:223], v[2:5]
	v_mfma_f32_16x16x32_f16 v[30:33], v[232:235], v[200:203], v[30:33]
	v_mfma_f32_16x16x32_f16 v[26:29], v[240:243], v[200:203], v[26:29]
	v_mfma_f32_16x16x32_f16 v[22:25], v[232:235], v[208:211], v[22:25]
	v_mfma_f32_16x16x32_f16 v[18:21], v[240:243], v[208:211], v[18:21]
	v_mfma_f32_16x16x32_f16 v[14:17], v[232:235], v[216:219], v[14:17]
	v_mfma_f32_16x16x32_f16 v[10:13], v[240:243], v[216:219], v[10:13]
	v_mfma_f32_16x16x32_f16 v[6:9], v[232:235], v[224:227], v[6:9]
	v_mfma_f32_16x16x32_f16 v[2:5], v[240:243], v[224:227], v[2:5]
	s_setprio 0
	s_barrier
	ds_read_b128 v[168:171], v133
	ds_read_b128 v[172:175], v133 offset:1024
	ds_read_b128 v[176:179], v133 offset:2048
	ds_read_b128 v[192:195], v133 offset:3072
	s_mov_b32 s56, s88
	s_mov_b32 m0, s56
	s_mov_b32 s56, s89
	ds_read_b128 v[196:199], v150 offset:32768
	ds_read_b128 v[200:203], v150 offset:33792
	ds_read_b128 v[204:207], v149 offset:32768
	ds_read_b128 v[208:211], v149 offset:33792
	ds_read_b128 v[212:215], v148 offset:32768
	ds_read_b128 v[216:219], v148 offset:33792
	ds_read_b128 v[220:223], v147 offset:32768
	ds_read_b128 v[224:227], v147 offset:33792
	s_add_u32 s100, s96, s30
	s_addc_u32 s101, s97, s31
	global_load_lds_dwordx4 v254, s[100:101]
	s_mov_b32 m0, s56
	s_nop 0
	global_load_lds_dwordx4 v255, s[100:101]
	s_waitcnt lgkmcnt(8)
	s_barrier
	s_waitcnt lgkmcnt(0)
	s_setprio 1
	s_waitcnt lgkmcnt(0)
	v_mfma_f32_16x16x32_f16 v[126:129], v[168:171], v[196:199], v[126:129]
	v_mfma_f32_16x16x32_f16 v[122:125], v[176:179], v[196:199], v[122:125]
	v_mfma_f32_16x16x32_f16 v[118:121], v[168:171], v[204:207], v[118:121]
	v_mfma_f32_16x16x32_f16 v[114:117], v[176:179], v[204:207], v[114:117]
	v_mfma_f32_16x16x32_f16 v[110:113], v[168:171], v[212:215], v[110:113]
	v_mfma_f32_16x16x32_f16 v[106:109], v[176:179], v[212:215], v[106:109]
	v_mfma_f32_16x16x32_f16 v[102:105], v[168:171], v[220:223], v[102:105]
	v_mfma_f32_16x16x32_f16 v[98:101], v[176:179], v[220:223], v[98:101]
	v_mfma_f32_16x16x32_f16 v[126:129], v[172:175], v[200:203], v[126:129]
	v_mfma_f32_16x16x32_f16 v[122:125], v[192:195], v[200:203], v[122:125]
	v_mfma_f32_16x16x32_f16 v[118:121], v[172:175], v[208:211], v[118:121]
	v_mfma_f32_16x16x32_f16 v[114:117], v[192:195], v[208:211], v[114:117]
	v_mfma_f32_16x16x32_f16 v[110:113], v[172:175], v[216:219], v[110:113]
	v_mfma_f32_16x16x32_f16 v[106:109], v[192:195], v[216:219], v[106:109]
	v_mfma_f32_16x16x32_f16 v[102:105], v[172:175], v[224:227], v[102:105]
	v_mfma_f32_16x16x32_f16 v[98:101], v[192:195], v[224:227], v[98:101]
	s_setprio 0
	s_barrier
	s_mov_b32 s56, s90
	s_mov_b32 m0, s56
	s_mov_b32 s56, s91
	ds_read_b128 v[228:231], v131
	ds_read_b128 v[232:235], v131 offset:1024
	ds_read_b128 v[236:239], v131 offset:2048
	ds_read_b128 v[240:243], v131 offset:3072
	s_add_u32 s100, s98, s52
	s_addc_u32 s101, s99, s53
	global_load_lds_dwordx4 v254, s[100:101]
	s_mov_b32 m0, s56
	s_nop 0
	global_load_lds_dwordx4 v255, s[100:101]
	s_barrier
	s_waitcnt lgkmcnt(0)
	s_setprio 1
	s_waitcnt lgkmcnt(0)
	v_mfma_f32_16x16x32_f16 v[94:97], v[228:231], v[196:199], v[94:97]
	v_mfma_f32_16x16x32_f16 v[90:93], v[236:239], v[196:199], v[90:93]
	v_mfma_f32_16x16x32_f16 v[86:89], v[228:231], v[204:207], v[86:89]
	v_mfma_f32_16x16x32_f16 v[82:85], v[236:239], v[204:207], v[82:85]
	v_mfma_f32_16x16x32_f16 v[78:81], v[228:231], v[212:215], v[78:81]
	v_mfma_f32_16x16x32_f16 v[74:77], v[236:239], v[212:215], v[74:77]
	v_mfma_f32_16x16x32_f16 v[70:73], v[228:231], v[220:223], v[70:73]
	v_mfma_f32_16x16x32_f16 v[66:69], v[236:239], v[220:223], v[66:69]
	v_mfma_f32_16x16x32_f16 v[94:97], v[232:235], v[200:203], v[94:97]
	v_mfma_f32_16x16x32_f16 v[90:93], v[240:243], v[200:203], v[90:93]
	v_mfma_f32_16x16x32_f16 v[86:89], v[232:235], v[208:211], v[86:89]
	v_mfma_f32_16x16x32_f16 v[82:85], v[240:243], v[208:211], v[82:85]
	v_mfma_f32_16x16x32_f16 v[78:81], v[232:235], v[216:219], v[78:81]
	v_mfma_f32_16x16x32_f16 v[74:77], v[240:243], v[216:219], v[74:77]
	v_mfma_f32_16x16x32_f16 v[70:73], v[232:235], v[224:227], v[70:73]
	v_mfma_f32_16x16x32_f16 v[66:69], v[240:243], v[224:227], v[66:69]
	s_setprio 0
	s_mov_b32 s56, s92
	s_mov_b32 m0, s56
	s_mov_b32 s56, s93
	s_barrier
	ds_read_b128 v[196:199], v150 offset:49152
	ds_read_b128 v[200:203], v150 offset:50176
	ds_read_b128 v[204:207], v149 offset:49152
	ds_read_b128 v[208:211], v149 offset:50176
	ds_read_b128 v[212:215], v148 offset:49152
	ds_read_b128 v[216:219], v148 offset:50176
	ds_read_b128 v[220:223], v147 offset:49152
	ds_read_b128 v[224:227], v147 offset:50176
	s_add_u32 s100, s96, s52
	s_addc_u32 s101, s97, s53
	global_load_lds_dwordx4 v254, s[100:101]
	s_mov_b32 m0, s56
	s_nop 0
	global_load_lds_dwordx4 v255, s[100:101]
	s_barrier
	s_waitcnt lgkmcnt(0)
	s_setprio 1
	s_waitcnt lgkmcnt(0)
	v_mfma_f32_16x16x32_f16 v[62:65], v[168:171], v[196:199], v[62:65]
	v_mfma_f32_16x16x32_f16 v[58:61], v[176:179], v[196:199], v[58:61]
	v_mfma_f32_16x16x32_f16 v[54:57], v[168:171], v[204:207], v[54:57]
	v_mfma_f32_16x16x32_f16 v[50:53], v[176:179], v[204:207], v[50:53]
	v_mfma_f32_16x16x32_f16 v[46:49], v[168:171], v[212:215], v[46:49]
	v_mfma_f32_16x16x32_f16 v[42:45], v[176:179], v[212:215], v[42:45]
	v_mfma_f32_16x16x32_f16 v[38:41], v[168:171], v[220:223], v[38:41]
	v_mfma_f32_16x16x32_f16 v[34:37], v[176:179], v[220:223], v[34:37]
	v_mfma_f32_16x16x32_f16 v[62:65], v[172:175], v[200:203], v[62:65]
	v_mfma_f32_16x16x32_f16 v[58:61], v[192:195], v[200:203], v[58:61]
	v_mfma_f32_16x16x32_f16 v[54:57], v[172:175], v[208:211], v[54:57]
	v_mfma_f32_16x16x32_f16 v[50:53], v[192:195], v[208:211], v[50:53]
	v_mfma_f32_16x16x32_f16 v[46:49], v[172:175], v[216:219], v[46:49]
	v_mfma_f32_16x16x32_f16 v[42:45], v[192:195], v[216:219], v[42:45]
	v_mfma_f32_16x16x32_f16 v[38:41], v[172:175], v[224:227], v[38:41]
	v_mfma_f32_16x16x32_f16 v[34:37], v[192:195], v[224:227], v[34:37]
	s_setprio 0
	s_barrier
	s_mov_b32 s56, s94
	s_mov_b32 m0, s56
	s_mov_b32 s56, s95
	s_add_u32 s100, s98, s54
	s_addc_u32 s101, s99, s55
	global_load_lds_dwordx4 v254, s[100:101]
	s_mov_b32 m0, s56
	s_nop 0
	global_load_lds_dwordx4 v255, s[100:101]
	s_waitcnt vmcnt(6)
	s_barrier
	s_setprio 1
	v_mfma_f32_16x16x32_f16 v[30:33], v[228:231], v[196:199], v[30:33]
	v_mfma_f32_16x16x32_f16 v[26:29], v[236:239], v[196:199], v[26:29]
	v_mfma_f32_16x16x32_f16 v[22:25], v[228:231], v[204:207], v[22:25]
	v_mfma_f32_16x16x32_f16 v[18:21], v[236:239], v[204:207], v[18:21]
	v_mfma_f32_16x16x32_f16 v[14:17], v[228:231], v[212:215], v[14:17]
	v_mfma_f32_16x16x32_f16 v[10:13], v[236:239], v[212:215], v[10:13]
	v_mfma_f32_16x16x32_f16 v[6:9], v[228:231], v[220:223], v[6:9]
	v_mfma_f32_16x16x32_f16 v[2:5], v[236:239], v[220:223], v[2:5]
	v_mfma_f32_16x16x32_f16 v[30:33], v[232:235], v[200:203], v[30:33]
	v_mfma_f32_16x16x32_f16 v[26:29], v[240:243], v[200:203], v[26:29]
	v_mfma_f32_16x16x32_f16 v[22:25], v[232:235], v[208:211], v[22:25]
	v_mfma_f32_16x16x32_f16 v[18:21], v[240:243], v[208:211], v[18:21]
	v_mfma_f32_16x16x32_f16 v[14:17], v[232:235], v[216:219], v[14:17]
	v_mfma_f32_16x16x32_f16 v[10:13], v[240:243], v[216:219], v[10:13]
	v_mfma_f32_16x16x32_f16 v[6:9], v[232:235], v[224:227], v[6:9]
	v_mfma_f32_16x16x32_f16 v[2:5], v[240:243], v[224:227], v[2:5]
	s_setprio 0
	s_add_i32 s35, s35, 2
	s_add_u32 s2, s2, 0x100
	s_addc_u32 s3, s3, 0
	s_add_u32 s96, s96, 0x100
	s_addc_u32 s97, s97, 0
	s_add_u32 s98, s98, 0x100
	s_addc_u32 s99, s99, 0
	s_cmp_lt_u32 s35, 28
	s_barrier
	s_cbranch_scc1 .LBB5_9
	v_add_u32_e32 v143, 0xc000, v142
	s_add_u32 s0, s50, 0x80f80
	v_readfirstlane_b32 s2, v143
	s_addc_u32 s1, s51, 0
	s_mov_b32 m0, s2
	ds_read_b128 v[134:137], v165
	ds_read_b128 v[138:141], v165 offset:1024
	ds_read_b128 v[154:157], v165 offset:2048
	ds_read_b128 v[158:161], v165 offset:3072
	global_load_lds_dwordx4 v130, s[0:1]
	v_add_u32_e32 v130, 0xe000, v142
	s_nop 0
	v_readfirstlane_b32 s2, v130
	s_mov_b32 m0, s2
	s_nop 0
	global_load_lds_dwordx4 v132, s[0:1]
	ds_read_b128 v[142:145], v150
	ds_read_b128 v[166:169], v150 offset:1024
	ds_read_b128 v[170:173], v149
	ds_read_b128 v[174:177], v149 offset:1024
	ds_read_b128 v[192:195], v148
	ds_read_b128 v[196:199], v148 offset:1024
	ds_read_b128 v[200:203], v147
	ds_read_b128 v[204:207], v147 offset:1024
	s_barrier
	s_waitcnt lgkmcnt(0)
	s_setprio 1
	s_waitcnt lgkmcnt(0)
	v_mfma_f32_16x16x32_f16 v[126:129], v[134:137], v[142:145], v[126:129]
	v_mfma_f32_16x16x32_f16 v[122:125], v[154:157], v[142:145], v[122:125]
	v_mfma_f32_16x16x32_f16 v[118:121], v[134:137], v[170:173], v[118:121]
	v_mfma_f32_16x16x32_f16 v[114:117], v[154:157], v[170:173], v[114:117]
	v_mfma_f32_16x16x32_f16 v[110:113], v[134:137], v[192:195], v[110:113]
	v_mfma_f32_16x16x32_f16 v[106:109], v[154:157], v[192:195], v[106:109]
	v_mfma_f32_16x16x32_f16 v[102:105], v[134:137], v[200:203], v[102:105]
	v_mfma_f32_16x16x32_f16 v[98:101], v[154:157], v[200:203], v[98:101]
	v_mfma_f32_16x16x32_f16 v[126:129], v[138:141], v[166:169], v[126:129]
	v_mfma_f32_16x16x32_f16 v[122:125], v[158:161], v[166:169], v[122:125]
	v_mfma_f32_16x16x32_f16 v[118:121], v[138:141], v[174:177], v[118:121]
	v_mfma_f32_16x16x32_f16 v[114:117], v[158:161], v[174:177], v[114:117]
	v_mfma_f32_16x16x32_f16 v[110:113], v[138:141], v[196:199], v[110:113]
	v_mfma_f32_16x16x32_f16 v[106:109], v[158:161], v[196:199], v[106:109]
	v_mfma_f32_16x16x32_f16 v[102:105], v[138:141], v[204:207], v[102:105]
	v_mfma_f32_16x16x32_f16 v[98:101], v[158:161], v[204:207], v[98:101]
	s_setprio 0
	s_barrier
	ds_read_b128 v[208:211], v163
	ds_read_b128 v[212:215], v163 offset:1024
	ds_read_b128 v[216:219], v163 offset:2048
	ds_read_b128 v[220:223], v163 offset:3072
	s_barrier
	s_waitcnt lgkmcnt(0)
	s_setprio 1
	s_waitcnt lgkmcnt(0)
	v_mfma_f32_16x16x32_f16 v[86:89], v[208:211], v[170:173], v[86:89]
	v_mfma_f32_16x16x32_f16 v[82:85], v[216:219], v[170:173], v[82:85]
	v_mfma_f32_16x16x32_f16 v[78:81], v[208:211], v[192:195], v[78:81]
	v_mfma_f32_16x16x32_f16 v[74:77], v[216:219], v[192:195], v[74:77]
	v_mfma_f32_16x16x32_f16 v[70:73], v[208:211], v[200:203], v[70:73]
	v_mfma_f32_16x16x32_f16 v[66:69], v[216:219], v[200:203], v[66:69]
	v_mfma_f32_16x16x32_f16 v[94:97], v[208:211], v[142:145], v[94:97]
	v_mfma_f32_16x16x32_f16 v[90:93], v[216:219], v[142:145], v[90:93]
	v_mfma_f32_16x16x32_f16 v[86:89], v[212:215], v[174:177], v[86:89]
	v_mfma_f32_16x16x32_f16 v[82:85], v[220:223], v[174:177], v[82:85]
	v_mfma_f32_16x16x32_f16 v[78:81], v[212:215], v[196:199], v[78:81]
	v_mfma_f32_16x16x32_f16 v[74:77], v[220:223], v[196:199], v[74:77]
	v_mfma_f32_16x16x32_f16 v[70:73], v[212:215], v[204:207], v[70:73]
	v_mfma_f32_16x16x32_f16 v[66:69], v[220:223], v[204:207], v[66:69]
	v_mfma_f32_16x16x32_f16 v[224:227], v[212:215], v[166:169], v[94:97]
	v_mfma_f32_16x16x32_f16 v[166:169], v[220:223], v[166:169], v[90:93]
	s_setprio 0
	s_barrier
	s_nop 0
	ds_read_b128 v[90:93], v150 offset:16384
	ds_read_b128 v[94:97], v150 offset:17408
	ds_read_b128 v[142:145], v149 offset:16384
	ds_read_b128 v[170:173], v149 offset:17408
	ds_read_b128 v[174:177], v148 offset:16384
	ds_read_b128 v[192:195], v148 offset:17408
	ds_read_b128 v[196:199], v147 offset:16384
	ds_read_b128 v[200:203], v147 offset:17408
	s_waitcnt vmcnt(4)
	s_barrier
	s_waitcnt lgkmcnt(0)
	s_setprio 1
	s_waitcnt lgkmcnt(0)
	v_mfma_f32_16x16x32_f16 v[62:65], v[134:137], v[90:93], v[62:65]
	v_mfma_f32_16x16x32_f16 v[58:61], v[154:157], v[90:93], v[58:61]
	v_mfma_f32_16x16x32_f16 v[54:57], v[134:137], v[142:145], v[54:57]
	v_mfma_f32_16x16x32_f16 v[50:53], v[154:157], v[142:145], v[50:53]
	v_mfma_f32_16x16x32_f16 v[46:49], v[134:137], v[174:177], v[46:49]
	v_mfma_f32_16x16x32_f16 v[42:45], v[154:157], v[174:177], v[42:45]
	v_mfma_f32_16x16x32_f16 v[38:41], v[134:137], v[196:199], v[38:41]
	v_mfma_f32_16x16x32_f16 v[62:65], v[138:141], v[94:97], v[62:65]
	v_mfma_f32_16x16x32_f16 v[58:61], v[158:161], v[94:97], v[58:61]
	v_mfma_f32_16x16x32_f16 v[54:57], v[138:141], v[170:173], v[54:57]
	v_mfma_f32_16x16x32_f16 v[50:53], v[158:161], v[170:173], v[50:53]
	v_mfma_f32_16x16x32_f16 v[46:49], v[138:141], v[192:195], v[46:49]
	v_mfma_f32_16x16x32_f16 v[42:45], v[158:161], v[192:195], v[42:45]
	v_mfma_f32_16x16x32_f16 v[38:41], v[138:141], v[200:203], v[38:41]
	v_mfma_f32_16x16x32_f16 v[34:37], v[154:157], v[196:199], v[34:37]
	v_mfma_f32_16x16x32_f16 v[34:37], v[158:161], v[200:203], v[34:37]
	s_setprio 0
	s_setprio 1
	v_mfma_f32_16x16x32_f16 v[30:33], v[208:211], v[90:93], v[30:33]
	v_mfma_f32_16x16x32_f16 v[6:9], v[208:211], v[196:199], v[6:9]
	v_mfma_f32_16x16x32_f16 v[2:5], v[216:219], v[196:199], v[2:5]
	v_mfma_f32_16x16x32_f16 v[30:33], v[212:215], v[94:97], v[30:33]
	v_mfma_f32_16x16x32_f16 v[26:29], v[216:219], v[90:93], v[26:29]
	v_mfma_f32_16x16x32_f16 v[22:25], v[208:211], v[142:145], v[22:25]
	v_mfma_f32_16x16x32_f16 v[18:21], v[216:219], v[142:145], v[18:21]
	v_mfma_f32_16x16x32_f16 v[14:17], v[208:211], v[174:177], v[14:17]
	v_mfma_f32_16x16x32_f16 v[10:13], v[216:219], v[174:177], v[10:13]
	v_mfma_f32_16x16x32_f16 v[6:9], v[212:215], v[200:203], v[6:9]
	v_mfma_f32_16x16x32_f16 v[2:5], v[220:223], v[200:203], v[2:5]
	v_mfma_f32_16x16x32_f16 v[26:29], v[220:223], v[94:97], v[26:29]
	v_mfma_f32_16x16x32_f16 v[154:157], v[212:215], v[170:173], v[22:25]
	v_mfma_f32_16x16x32_f16 v[18:21], v[220:223], v[170:173], v[18:21]
	v_mfma_f32_16x16x32_f16 v[158:161], v[212:215], v[192:195], v[14:17]
	v_mfma_f32_16x16x32_f16 v[10:13], v[220:223], v[192:195], v[10:13]
	s_setprio 0
	s_barrier
	ds_read_b128 v[14:17], v133
	ds_read_b128 v[22:25], v133 offset:1024
	ds_read_b128 v[170:173], v133 offset:2048
	ds_read_b128 v[174:177], v133 offset:3072
	ds_read_b128 v[192:195], v150 offset:32768
	ds_read_b128 v[196:199], v150 offset:33792
	ds_read_b128 v[200:203], v149 offset:32768
	ds_read_b128 v[204:207], v149 offset:33792
	ds_read_b128 v[208:211], v148 offset:32768
	ds_read_b128 v[212:215], v148 offset:33792
	ds_read_b128 v[216:219], v147 offset:32768
	ds_read_b128 v[220:223], v147 offset:33792
	s_waitcnt vmcnt(2)
	s_barrier
	s_waitcnt lgkmcnt(0)
	s_setprio 1
	s_waitcnt lgkmcnt(0)
	v_mfma_f32_16x16x32_f16 v[90:93], v[14:17], v[192:195], v[126:129]
	v_mfma_f32_16x16x32_f16 v[142:145], v[22:25], v[196:199], v[90:93]
	v_mfma_f32_16x16x32_f16 v[90:93], v[170:173], v[192:195], v[122:125]
	v_mfma_f32_16x16x32_f16 v[138:141], v[174:177], v[196:199], v[90:93]
	v_mfma_f32_16x16x32_f16 v[90:93], v[14:17], v[200:203], v[118:121]
	v_mfma_f32_16x16x32_f16 v[126:129], v[22:25], v[204:207], v[90:93]
	v_mfma_f32_16x16x32_f16 v[90:93], v[170:173], v[200:203], v[114:117]
	v_mfma_f32_16x16x32_f16 v[122:125], v[174:177], v[204:207], v[90:93]
	v_mfma_f32_16x16x32_f16 v[90:93], v[14:17], v[208:211], v[110:113]
	v_mfma_f32_16x16x32_f16 v[110:113], v[22:25], v[212:215], v[90:93]
	v_mfma_f32_16x16x32_f16 v[90:93], v[170:173], v[208:211], v[106:109]
	v_mfma_f32_16x16x32_f16 v[106:109], v[174:177], v[212:215], v[90:93]
	v_mfma_f32_16x16x32_f16 v[90:93], v[14:17], v[216:219], v[102:105]
	v_mfma_f32_16x16x32_f16 v[94:97], v[22:25], v[220:223], v[90:93]
	v_mfma_f32_16x16x32_f16 v[90:93], v[170:173], v[216:219], v[98:101]
	v_mfma_f32_16x16x32_f16 v[90:93], v[174:177], v[220:223], v[90:93]
	s_setprio 0
	s_barrier
	ds_read_b128 v[228:231], v131
	ds_read_b128 v[232:235], v131 offset:1024
	ds_read_b128 v[236:239], v131 offset:2048
	ds_read_b128 v[240:243], v131 offset:3072
	s_waitcnt vmcnt(0)
	s_barrier
	s_waitcnt lgkmcnt(0)
	s_setprio 1
	s_waitcnt lgkmcnt(0)
	v_mfma_f32_16x16x32_f16 v[98:101], v[228:231], v[192:195], v[224:227]
	v_mfma_f32_16x16x32_f16 v[134:137], v[232:235], v[196:199], v[98:101]
	v_mfma_f32_16x16x32_f16 v[98:101], v[236:239], v[192:195], v[166:169]
	v_mfma_f32_16x16x32_f16 v[86:89], v[228:231], v[200:203], v[86:89]
	v_mfma_f32_16x16x32_f16 v[82:85], v[236:239], v[200:203], v[82:85]
	v_mfma_f32_16x16x32_f16 v[78:81], v[228:231], v[208:211], v[78:81]
	v_mfma_f32_16x16x32_f16 v[74:77], v[236:239], v[208:211], v[74:77]
	v_mfma_f32_16x16x32_f16 v[70:73], v[228:231], v[216:219], v[70:73]
	v_mfma_f32_16x16x32_f16 v[66:69], v[236:239], v[216:219], v[66:69]
	v_mfma_f32_16x16x32_f16 v[130:133], v[240:243], v[196:199], v[98:101]
	v_mfma_f32_16x16x32_f16 v[118:121], v[232:235], v[204:207], v[86:89]
	v_mfma_f32_16x16x32_f16 v[114:117], v[240:243], v[204:207], v[82:85]
	v_mfma_f32_16x16x32_f16 v[102:105], v[232:235], v[212:215], v[78:81]
	v_mfma_f32_16x16x32_f16 v[98:101], v[240:243], v[212:215], v[74:77]
	v_mfma_f32_16x16x32_f16 v[86:89], v[232:235], v[220:223], v[70:73]
	v_mfma_f32_16x16x32_f16 v[82:85], v[240:243], v[220:223], v[66:69]
	s_setprio 0
	s_barrier
	s_nop 0
	ds_read_b128 v[66:69], v150 offset:49152
	ds_read_b128 v[166:169], v150 offset:50176
	ds_read_b128 v[192:195], v149 offset:49152
	ds_read_b128 v[196:199], v149 offset:50176
	ds_read_b128 v[200:203], v148 offset:49152
	ds_read_b128 v[148:151], v148 offset:50176
	ds_read_b128 v[204:207], v147 offset:49152
	ds_read_b128 v[208:211], v147 offset:50176
	s_barrier
	s_waitcnt lgkmcnt(0)
	s_setprio 1
	s_waitcnt lgkmcnt(0)
	v_mfma_f32_16x16x32_f16 v[62:65], v[14:17], v[66:69], v[62:65]
	v_mfma_f32_16x16x32_f16 v[54:57], v[14:17], v[192:195], v[54:57]
	v_mfma_f32_16x16x32_f16 v[46:49], v[14:17], v[200:203], v[46:49]
	v_mfma_f32_16x16x32_f16 v[14:17], v[14:17], v[204:207], v[38:41]
	v_mfma_f32_16x16x32_f16 v[78:81], v[22:25], v[166:169], v[62:65]
	v_mfma_f32_16x16x32_f16 v[58:61], v[170:173], v[66:69], v[58:61]
	v_mfma_f32_16x16x32_f16 v[62:65], v[22:25], v[196:199], v[54:57]
	v_mfma_f32_16x16x32_f16 v[50:53], v[170:173], v[192:195], v[50:53]
	v_mfma_f32_16x16x32_f16 v[46:49], v[22:25], v[148:151], v[46:49]
	v_mfma_f32_16x16x32_f16 v[42:45], v[170:173], v[200:203], v[42:45]
	v_mfma_f32_16x16x32_f16 v[22:25], v[22:25], v[208:211], v[14:17]
	v_mfma_f32_16x16x32_f16 v[14:17], v[170:173], v[204:207], v[34:37]
	v_mfma_f32_16x16x32_f16 v[74:77], v[174:177], v[166:169], v[58:61]
	v_mfma_f32_16x16x32_f16 v[58:61], v[174:177], v[196:199], v[50:53]
	v_mfma_f32_16x16x32_f16 v[42:45], v[174:177], v[148:151], v[42:45]
	v_mfma_f32_16x16x32_f16 v[14:17], v[174:177], v[208:211], v[14:17]
	s_setprio 0
	s_setprio 1
	v_mfma_f32_16x16x32_f16 v[26:29], v[236:239], v[66:69], v[26:29]
	v_mfma_f32_16x16x32_f16 v[18:21], v[236:239], v[192:195], v[18:21]
	v_mfma_f32_16x16x32_f16 v[30:33], v[228:231], v[66:69], v[30:33]
	v_mfma_f32_16x16x32_f16 v[66:69], v[240:243], v[166:169], v[26:29]
	v_mfma_f32_16x16x32_f16 v[26:29], v[228:231], v[192:195], v[154:157]
	v_mfma_f32_16x16x32_f16 v[50:53], v[240:243], v[196:199], v[18:21]
	v_mfma_f32_16x16x32_f16 v[18:21], v[228:231], v[200:203], v[158:161]
	v_mfma_f32_16x16x32_f16 v[10:13], v[236:239], v[200:203], v[10:13]
	v_mfma_f32_16x16x32_f16 v[6:9], v[228:231], v[204:207], v[6:9]
	v_mfma_f32_16x16x32_f16 v[2:5], v[236:239], v[204:207], v[2:5]
	v_mfma_f32_16x16x32_f16 v[70:73], v[232:235], v[166:169], v[30:33]
	v_mfma_f32_16x16x32_f16 v[54:57], v[232:235], v[196:199], v[26:29]
	v_mfma_f32_16x16x32_f16 v[38:41], v[232:235], v[148:151], v[18:21]
	v_mfma_f32_16x16x32_f16 v[30:33], v[240:243], v[148:151], v[10:13]
	v_mfma_f32_16x16x32_f16 v[6:9], v[232:235], v[208:211], v[6:9]
	v_mfma_f32_16x16x32_f16 v[2:5], v[240:243], v[208:211], v[2:5]
	s_setprio 0
	s_movk_i32 s0, 0x100
	v_cmp_gt_u32_e32 vcc, s0, v0
	s_barrier
	s_and_saveexec_b64 s[0:1], vcc
	s_cbranch_execz .LBB5_12
	s_barrier

	.amdhsa_kernel _Z8k_expertPKDF16_S0_PKfPcPiS0_S2_S2_S2_S2_PfS5_S4_S2_S2_S2_S2_S5_S2_S2_S2_
		.amdhsa_group_segment_fixed_size 0
		.amdhsa_private_segment_fixed_size 0
		.amdhsa_kernarg_size 168
		.amdhsa_user_sgpr_count 2
		.amdhsa_user_sgpr_dispatch_ptr 0
		.amdhsa_user_sgpr_queue_ptr 0
		.amdhsa_user_sgpr_kernarg_segment_ptr 1
		.amdhsa_user_sgpr_dispatch_id 0
		.amdhsa_user_sgpr_kernarg_preload_length 0
		.amdhsa_user_sgpr_kernarg_preload_offset 0
		.amdhsa_user_sgpr_private_segment_size 0
		.amdhsa_uses_dynamic_stack 0
		.amdhsa_enable_private_segment 0
		.amdhsa_system_sgpr_workgroup_id_x 1
		.amdhsa_system_sgpr_workgroup_id_y 0
		.amdhsa_system_sgpr_workgroup_id_z 0
		.amdhsa_system_sgpr_workgroup_info 0
		.amdhsa_system_vgpr_workitem_id 0
		.amdhsa_next_free_vgpr 256
		.amdhsa_next_free_sgpr 102
		.amdhsa_accum_offset 256
		.amdhsa_reserve_vcc 1
		.amdhsa_float_round_mode_32 0
		.amdhsa_float_round_mode_16_64 0
		.amdhsa_float_denorm_mode_32 3
		.amdhsa_float_denorm_mode_16_64 3
		.amdhsa_dx10_clamp 1
		.amdhsa_ieee_mode 1
		.amdhsa_fp16_overflow 0
		.amdhsa_tg_split 0
		.amdhsa_exception_fp_ieee_invalid_op 0
		.amdhsa_exception_fp_denorm_src 0
		.amdhsa_exception_fp_ieee_div_zero 0
		.amdhsa_exception_fp_ieee_overflow 0
		.amdhsa_exception_fp_ieee_underflow 0
		.amdhsa_exception_fp_ieee_inexact 0
		.amdhsa_exception_int_div_zero 0
	.end_amdhsa_kernel

amdhsa.kernels:
  - .agpr_count:     0
    .args:
      - .actual_access:  read_only
        .address_space:  global
        .offset:         0
        .size:           8
        .value_kind:     global_buffer
      - .actual_access:  read_only
        .address_space:  global
        .offset:         8
        .size:           8
        .value_kind:     global_buffer
      - .actual_access:  read_only
        .address_space:  global
        .offset:         16
        .size:           8
        .value_kind:     global_buffer
      - .actual_access:  write_only
        .address_space:  global
        .offset:         24
        .size:           8
        .value_kind:     global_buffer
      - .actual_access:  write_only
        .address_space:  global
        .offset:         32
        .size:           8
        .value_kind:     global_buffer
      - .actual_access:  read_only
        .address_space:  global
        .offset:         40
        .size:           8
        .value_kind:     global_buffer
      - .actual_access:  read_only
        .address_space:  global
        .offset:         48
        .size:           8
        .value_kind:     global_buffer
      - .actual_access:  read_only
        .address_space:  global
        .offset:         56
        .size:           8
        .value_kind:     global_buffer
      - .actual_access:  read_only
        .address_space:  global
        .offset:         64
        .size:           8
        .value_kind:     global_buffer
      - .actual_access:  read_only
        .address_space:  global
        .offset:         72
        .size:           8
        .value_kind:     global_buffer
      - .actual_access:  read_only
        .address_space:  global
        .offset:         80
        .size:           8
        .value_kind:     global_buffer
    .group_segment_fixed_size: 16384
    .kernarg_segment_align: 8
    .kernarg_segment_size: 88
    .language:       OpenCL C
    .language_version:
      - 2
      - 0
    .max_flat_workgroup_size: 768
    .name:           _Z9k_router2PKfPKDF16_S0_PDF16_PfPiS0_S0_S4_S5_S4_
    .private_segment_fixed_size: 0
    .sgpr_count:     21
    .sgpr_spill_count: 0
    .symbol:         _Z9k_router2PKfPKDF16_S0_PDF16_PfPiS0_S0_S4_S5_S4_.kd
    .uniform_work_group_size: 1
    .uses_dynamic_stack: false
    .vgpr_count:     168
    .vgpr_spill_count: 0
    .wavefront_size: 64
  - .agpr_count:     0
    .args:
      - .actual_access:  read_only
        .address_space:  global
        .offset:         0
        .size:           8
        .value_kind:     global_buffer
      - .actual_access:  read_only
        .address_space:  global
        .offset:         8
        .size:           8
        .value_kind:     global_buffer
      - .actual_access:  read_only
        .address_space:  global
        .offset:         16
        .size:           8
        .value_kind:     global_buffer
      - .actual_access:  write_only
        .address_space:  global
        .offset:         24
        .size:           8
        .value_kind:     global_buffer
      - .actual_access:  write_only
        .address_space:  global
        .offset:         32
        .size:           8
        .value_kind:     global_buffer
      - .actual_access:  write_only
        .address_space:  global
        .offset:         40
        .size:           8
        .value_kind:     global_buffer
    .group_segment_fixed_size: 256
    .kernarg_segment_align: 8
    .kernarg_segment_size: 48
    .language:       OpenCL C
    .language_version:
      - 2
      - 0
    .max_flat_workgroup_size: 256
    .name:           _Z6k_gatePKfS0_S0_PfPiS1_
    .private_segment_fixed_size: 0
    .sgpr_count:     26
    .sgpr_spill_count: 0
    .symbol:         _Z6k_gatePKfS0_S0_PfPiS1_.kd
    .uniform_work_group_size: 1
    .uses_dynamic_stack: false
    .vgpr_count:     51
    .vgpr_spill_count: 0
    .wavefront_size: 64
  - .agpr_count:     0
    .args:
      - .actual_access:  read_only
        .address_space:  global
        .offset:         0
        .size:           8
        .value_kind:     global_buffer
      - .actual_access:  write_only
        .address_space:  global
        .offset:         8
        .size:           8
        .value_kind:     global_buffer
      - .actual_access:  read_only
        .address_space:  global
        .offset:         16
        .size:           8
        .value_kind:     global_buffer
      - .actual_access:  read_only
        .address_space:  global
        .offset:         24
        .size:           8
        .value_kind:     global_buffer
      - .actual_access:  read_only
        .address_space:  global
        .offset:         32
        .size:           8
        .value_kind:     global_buffer
      - .actual_access:  write_only
        .address_space:  global
        .offset:         40
        .size:           8
        .value_kind:     global_buffer
      - .actual_access:  write_only
        .address_space:  global
        .offset:         48
        .size:           8
        .value_kind:     global_buffer
      - .actual_access:  write_only
        .address_space:  global
        .offset:         56
        .size:           8
        .value_kind:     global_buffer
      - .actual_access:  write_only
        .address_space:  global
        .offset:         64
        .size:           8
        .value_kind:     global_buffer
      - .actual_access:  write_only
        .address_space:  global
        .offset:         72
        .size:           8
        .value_kind:     global_buffer
    .group_segment_fixed_size: 16640
    .kernarg_segment_align: 8
    .kernarg_segment_size: 80
    .language:       OpenCL C
    .language_version:
      - 2
      - 0
    .max_flat_workgroup_size: 256
    .name:           _Z10k_prep_allPKfPDF16_S0_S0_S0_S1_S1_PiS2_S2_
    .private_segment_fixed_size: 0
    .sgpr_count:     20
    .sgpr_spill_count: 0
    .symbol:         _Z10k_prep_allPKfPDF16_S0_S0_S0_S1_S1_PiS2_S2_.kd
    .uniform_work_group_size: 1
    .uses_dynamic_stack: false
    .vgpr_count:     37
    .vgpr_spill_count: 0
    .wavefront_size: 64
  - .agpr_count:     0
    .args:
      - .address_space:  global
        .offset:         0
        .size:           8
        .value_kind:     global_buffer
      - .address_space:  global
        .offset:         8
        .size:           8
        .value_kind:     global_buffer
      - .actual_access:  read_only
        .address_space:  global
        .offset:         16
        .size:           8
        .value_kind:     global_buffer
      - .actual_access:  read_only
        .address_space:  global
        .offset:         24
        .size:           8
        .value_kind:     global_buffer
      - .actual_access:  write_only
        .address_space:  global
        .offset:         32
        .size:           8
        .value_kind:     global_buffer
    .group_segment_fixed_size: 0
    .kernarg_segment_align: 8
    .kernarg_segment_size: 40
    .language:       OpenCL C
    .language_version:
      - 2
      - 0
    .max_flat_workgroup_size: 512
    .name:           _Z7k_gemm1PKDF16_S0_PKfPKiPDF16_
    .private_segment_fixed_size: 0
    .sgpr_count:     36
    .sgpr_spill_count: 0
    .symbol:         _Z7k_gemm1PKDF16_S0_PKfPKiPDF16_.kd
    .uniform_work_group_size: 1
    .uses_dynamic_stack: false
    .vgpr_count:     240
    .vgpr_spill_count: 0
    .wavefront_size: 64
  - .agpr_count:     0
    .args:
      - .address_space:  global
        .offset:         0
        .size:           8
        .value_kind:     global_buffer
      - .actual_access:  read_only
        .address_space:  global
        .offset:         8
        .size:           8
        .value_kind:     global_buffer
      - .actual_access:  read_only
        .address_space:  global
        .offset:         16
        .size:           8
        .value_kind:     global_buffer
      - .actual_access:  read_only
        .address_space:  global
        .offset:         24
        .size:           8
        .value_kind:     global_buffer
      - .actual_access:  read_only
        .address_space:  global
        .offset:         32
        .size:           8
        .value_kind:     global_buffer
      - .actual_access:  read_only
        .address_space:  global
        .offset:         40
        .size:           8
        .value_kind:     global_buffer
      - .actual_access:  read_only
        .address_space:  global
        .offset:         48
        .size:           8
        .value_kind:     global_buffer
      - .actual_access:  write_only
        .address_space:  global
        .offset:         56
        .size:           8
        .value_kind:     global_buffer
      - .actual_access:  write_only
        .address_space:  global
        .offset:         64
        .size:           8
        .value_kind:     global_buffer
    .group_segment_fixed_size: 0
    .kernarg_segment_align: 8
    .kernarg_segment_size: 72
    .language:       OpenCL C
    .language_version:
      - 2
      - 0
    .max_flat_workgroup_size: 512
    .name:           _Z11k_gemm2poolPKDF16_S0_PKfS2_S2_S2_PKiPfS5_
    .private_segment_fixed_size: 0
    .sgpr_count:     32
    .sgpr_spill_count: 0
    .symbol:         _Z11k_gemm2poolPKDF16_S0_PKfS2_S2_S2_PKiPfS5_.kd
    .uniform_work_group_size: 1
    .uses_dynamic_stack: false
    .vgpr_count:     198
    .vgpr_spill_count: 0
    .wavefront_size: 64
  - .agpr_count:     0
    .args:
      - .address_space:  global
        .offset:         0
        .size:           8
        .value_kind:     global_buffer
      - .address_space:  global
        .offset:         8
        .size:           8
        .value_kind:     global_buffer
      - .actual_access:  read_only
        .address_space:  global
        .offset:         16
        .size:           8
        .value_kind:     global_buffer
      - .address_space:  global
        .offset:         24
        .size:           8
        .value_kind:     global_buffer
      - .address_space:  global
        .offset:         32
        .size:           8
        .value_kind:     global_buffer
      - .actual_access:  read_only
        .address_space:  global
        .offset:         40
        .size:           8
        .value_kind:     global_buffer
      - .actual_access:  read_only
        .address_space:  global
        .offset:         48
        .size:           8
        .value_kind:     global_buffer
      - .actual_access:  read_only
        .address_space:  global
        .offset:         56
        .size:           8
        .value_kind:     global_buffer
      - .actual_access:  read_only
        .address_space:  global
        .offset:         64
        .size:           8
        .value_kind:     global_buffer
      - .actual_access:  read_only
        .address_space:  global
        .offset:         72
        .size:           8
        .value_kind:     global_buffer
      - .address_space:  global
        .offset:         80
        .size:           8
        .value_kind:     global_buffer
      - .address_space:  global
        .offset:         88
        .size:           8
        .value_kind:     global_buffer
      - .address_space:  global
        .offset:         96
        .size:           8
        .value_kind:     global_buffer
      - .actual_access:  read_only
        .address_space:  global
        .offset:         104
        .size:           8
        .value_kind:     global_buffer
      - .actual_access:  read_only
        .address_space:  global
        .offset:         112
        .size:           8
        .value_kind:     global_buffer
      - .actual_access:  read_only
        .address_space:  global
        .offset:         120
        .size:           8
        .value_kind:     global_buffer
      - .actual_access:  read_only
        .address_space:  global
        .offset:         128
        .size:           8
        .value_kind:     global_buffer
      - .actual_access:  write_only
        .address_space:  global
        .offset:         136
        .size:           8
        .value_kind:     global_buffer
      - .actual_access:  read_only
        .address_space:  global
        .offset:         144
        .size:           8
        .value_kind:     global_buffer
      - .actual_access:  read_only
        .address_space:  global
        .offset:         152
        .size:           8
        .value_kind:     global_buffer
      - .actual_access:  read_only
        .address_space:  global
        .offset:         160
        .size:           8
        .value_kind:     global_buffer
    .group_segment_fixed_size: 0
    .kernarg_segment_align: 8
    .kernarg_segment_size: 168
    .language:       OpenCL C
    .language_version:
      - 2
      - 0
    .max_flat_workgroup_size: 512
    .name:           _Z8k_expertPKDF16_S0_PKfPcPiS0_S2_S2_S2_S2_PfS5_S4_S2_S2_S2_S2_S5_S2_S2_S2_
    .private_segment_fixed_size: 0
    .sgpr_count:     108
    .sgpr_spill_count: 0
    .symbol:         _Z8k_expertPKDF16_S0_PKfPcPiS0_S2_S2_S2_S2_PfS5_S4_S2_S2_S2_S2_S5_S2_S2_S2_.kd
    .uniform_work_group_size: 1
    .uses_dynamic_stack: false
    .vgpr_count:     256
    .vgpr_spill_count: 0
    .wavefront_size: 64
  - .agpr_count:     0
    .args:
      - .actual_access:  read_only
        .address_space:  global
        .offset:         0
        .size:           8
        .value_kind:     global_buffer
      - .actual_access:  read_only
        .address_space:  global
        .offset:         8
        .size:           8
        .value_kind:     global_buffer
      - .actual_access:  read_only
        .address_space:  global
        .offset:         16
        .size:           8
        .value_kind:     global_buffer
      - .actual_access:  read_only
        .address_space:  global
        .offset:         24
        .size:           8
        .value_kind:     global_buffer
      - .actual_access:  read_only
        .address_space:  global
        .offset:         32
        .size:           8
        .value_kind:     global_buffer
      - .actual_access:  read_only
        .address_space:  global
        .offset:         40
        .size:           8
        .value_kind:     global_buffer
      - .actual_access:  read_only
        .address_space:  global
        .offset:         48
        .size:           8
        .value_kind:     global_buffer
      - .actual_access:  read_only
        .address_space:  global
        .offset:         56
        .size:           8
        .value_kind:     global_buffer
      - .actual_access:  write_only
        .address_space:  global
        .offset:         64
        .size:           8
        .value_kind:     global_buffer
    .group_segment_fixed_size: 8768
    .kernarg_segment_align: 8
    .kernarg_segment_size: 72
    .language:       OpenCL C
    .language_version:
      - 2
      - 0
    .max_flat_workgroup_size: 1024
    .name:           _Z7k_finalPKfS0_S0_S0_S0_PKiS0_S0_Pf
    .private_segment_fixed_size: 0
    .sgpr_count:     24
    .sgpr_spill_count: 0
    .symbol:         _Z7k_finalPKfS0_S0_S0_S0_PKiS0_S0_Pf.kd
    .uniform_work_group_size: 1
    .uses_dynamic_stack: false
    .vgpr_count:     83
    .vgpr_spill_count: 0
    .wavefront_size: 64
